# speedup vs baseline: 1.0041x; 1.0002x over previous
.LBB4_11:
	ds_bpermute_b32 v74, v72, v55
	ds_bpermute_b32 v78, v72, v53
	ds_bpermute_b32 v100, v72, v55 offset:4
	ds_bpermute_b32 v79, v72, v53 offset:4
	ds_bpermute_b32 v104, v72, v55 offset:8
	ds_bpermute_b32 v112, v72, v53 offset:8
	ds_bpermute_b32 v108, v72, v55 offset:12
	ds_bpermute_b32 v113, v72, v53 offset:12
	v_add_u32_e32 v71, -4, v71
	v_cmp_ge_i32_e64 s[0:1], 0, v71
	v_add_u32_e32 v72, 16, v72
	s_waitcnt lgkmcnt(0)
	v_ashrrev_i32_e32 v75, 31, v74
	v_ashrrev_i32_e32 v101, 31, v100
	v_ashrrev_i32_e32 v105, 31, v104
	v_ashrrev_i32_e32 v109, 31, v108
	v_lshlrev_b64 v[74:75], 8, v[74:75]
	v_lshlrev_b64 v[100:101], 8, v[100:101]
	v_lshlrev_b64 v[104:105], 8, v[104:105]
	v_lshlrev_b64 v[108:109], 8, v[108:109]
	v_lshl_add_u64 v[74:75], v[50:51], 0, v[74:75]
	v_lshl_add_u64 v[100:101], v[50:51], 0, v[100:101]
	v_lshl_add_u64 v[104:105], v[50:51], 0, v[104:105]
	v_lshl_add_u64 v[108:109], v[50:51], 0, v[108:109]
	global_load_dwordx4 v[74:77], v[74:75], off
	global_load_dwordx4 v[100:103], v[100:101], off
	global_load_dwordx4 v[104:107], v[104:105], off
	global_load_dwordx4 v[108:111], v[108:109], off
	s_or_b64 s[22:23], s[0:1], s[22:23]
	s_waitcnt vmcnt(3)
	v_fmac_f32_e32 v34, v76, v78
	v_fmac_f32_e32 v35, v77, v78
	v_fmac_f32_e32 v36, v74, v78
	v_fmac_f32_e32 v37, v75, v78
	s_waitcnt vmcnt(2)
	v_fmac_f32_e32 v34, v102, v79
	v_fmac_f32_e32 v35, v103, v79
	v_fmac_f32_e32 v36, v100, v79
	v_fmac_f32_e32 v37, v101, v79
	s_waitcnt vmcnt(1)
	v_fmac_f32_e32 v34, v106, v112
	v_fmac_f32_e32 v35, v107, v112
	v_fmac_f32_e32 v36, v104, v112
	v_fmac_f32_e32 v37, v105, v112
	s_waitcnt vmcnt(0)
	v_fmac_f32_e32 v34, v110, v113
	v_fmac_f32_e32 v35, v111, v113
	v_fmac_f32_e32 v36, v108, v113
	v_fmac_f32_e32 v37, v109, v113
	s_andn2_b64 exec, exec, s[22:23]
	s_cbranch_execnz .LBB4_11
	s_or_b64 exec, exec, s[22:23]

	.amdhsa_kernel _Z10gcn_kernelPKiS0_S0_S0_PKfS2_S2_S2_Pf
		.amdhsa_group_segment_fixed_size 26624
		.amdhsa_private_segment_fixed_size 0
		.amdhsa_kernarg_size 72
		.amdhsa_user_sgpr_count 2
		.amdhsa_user_sgpr_dispatch_ptr 0
		.amdhsa_user_sgpr_queue_ptr 0
		.amdhsa_user_sgpr_kernarg_segment_ptr 1
		.amdhsa_user_sgpr_dispatch_id 0
		.amdhsa_user_sgpr_kernarg_preload_length 0
		.amdhsa_user_sgpr_kernarg_preload_offset 0
		.amdhsa_user_sgpr_private_segment_size 0
		.amdhsa_uses_dynamic_stack 0
		.amdhsa_enable_private_segment 0
		.amdhsa_system_sgpr_workgroup_id_x 1
		.amdhsa_system_sgpr_workgroup_id_y 0
		.amdhsa_system_sgpr_workgroup_id_z 0
		.amdhsa_system_sgpr_workgroup_info 0
		.amdhsa_system_vgpr_workitem_id 0
		.amdhsa_next_free_vgpr 120
		.amdhsa_next_free_sgpr 91
		.amdhsa_accum_offset 120
		.amdhsa_reserve_vcc 1
		.amdhsa_float_round_mode_32 0
		.amdhsa_float_round_mode_16_64 0
		.amdhsa_float_denorm_mode_32 3
		.amdhsa_float_denorm_mode_16_64 3
		.amdhsa_dx10_clamp 1
		.amdhsa_ieee_mode 1
		.amdhsa_fp16_overflow 0
		.amdhsa_tg_split 0
		.amdhsa_exception_fp_ieee_invalid_op 0
		.amdhsa_exception_fp_denorm_src 0
		.amdhsa_exception_fp_ieee_div_zero 0
		.amdhsa_exception_fp_ieee_overflow 0
		.amdhsa_exception_fp_ieee_underflow 0
		.amdhsa_exception_fp_ieee_inexact 0
		.amdhsa_exception_int_div_zero 0
	.end_amdhsa_kernel

amdhsa.kernels:
  - .agpr_count:     0
    .args:
      - .actual_access:  write_only
        .address_space:  global
        .offset:         0
        .size:           8
        .value_kind:     global_buffer
      - .offset:         8
        .size:           4
        .value_kind:     by_value
      - .offset:         16
        .size:           4
        .value_kind:     hidden_block_count_x
      - .offset:         20
        .size:           4
        .value_kind:     hidden_block_count_y
      - .offset:         24
        .size:           4
        .value_kind:     hidden_block_count_z
      - .offset:         28
        .size:           2
        .value_kind:     hidden_group_size_x
      - .offset:         30
        .size:           2
        .value_kind:     hidden_group_size_y
      - .offset:         32
        .size:           2
        .value_kind:     hidden_group_size_z
      - .offset:         34
        .size:           2
        .value_kind:     hidden_remainder_x
      - .offset:         36
        .size:           2
        .value_kind:     hidden_remainder_y
      - .offset:         38
        .size:           2
        .value_kind:     hidden_remainder_z
      - .offset:         56
        .size:           8
        .value_kind:     hidden_global_offset_x
      - .offset:         64
        .size:           8
        .value_kind:     hidden_global_offset_y
      - .offset:         72
        .size:           8
        .value_kind:     hidden_global_offset_z
      - .offset:         80
        .size:           2
        .value_kind:     hidden_grid_dims
    .group_segment_fixed_size: 0
    .kernarg_segment_align: 8
    .kernarg_segment_size: 272
    .language:       OpenCL C
    .language_version:
      - 2
      - 0
    .max_flat_workgroup_size: 1024
    .name:           _Z11zero_kernelPDv4_fi
    .private_segment_fixed_size: 0
    .sgpr_count:     11
    .sgpr_spill_count: 0
    .symbol:         _Z11zero_kernelPDv4_fi.kd
    .uniform_work_group_size: 1
    .uses_dynamic_stack: false
    .vgpr_count:     6
    .vgpr_spill_count: 0
    .wavefront_size: 64
  - .agpr_count:     0
    .args:
      - .actual_access:  read_only
        .address_space:  global
        .offset:         0
        .size:           8
        .value_kind:     global_buffer
      - .actual_access:  read_only
        .address_space:  global
        .offset:         8
        .size:           8
        .value_kind:     global_buffer
      - .actual_access:  read_only
        .address_space:  global
        .offset:         16
        .size:           8
        .value_kind:     global_buffer
      - .actual_access:  read_only
        .address_space:  global
        .offset:         24
        .size:           8
        .value_kind:     global_buffer
      - .actual_access:  write_only
        .address_space:  global
        .offset:         32
        .size:           8
        .value_kind:     global_buffer
      - .actual_access:  read_only
        .address_space:  global
        .offset:         40
        .size:           8
        .value_kind:     global_buffer
      - .actual_access:  read_only
        .address_space:  global
        .offset:         48
        .size:           8
        .value_kind:     global_buffer
      - .address_space:  global
        .offset:         56
        .size:           8
        .value_kind:     global_buffer
      - .address_space:  global
        .offset:         64
        .size:           8
        .value_kind:     global_buffer
      - .address_space:  global
        .offset:         72
        .size:           8
        .value_kind:     global_buffer
      - .address_space:  global
        .offset:         80
        .size:           8
        .value_kind:     global_buffer
      - .offset:         88
        .size:           4
        .value_kind:     hidden_block_count_x
      - .offset:         92
        .size:           4
        .value_kind:     hidden_block_count_y
      - .offset:         96
        .size:           4
        .value_kind:     hidden_block_count_z
      - .offset:         100
        .size:           2
        .value_kind:     hidden_group_size_x
      - .offset:         102
        .size:           2
        .value_kind:     hidden_group_size_y
      - .offset:         104
        .size:           2
        .value_kind:     hidden_group_size_z
      - .offset:         106
        .size:           2
        .value_kind:     hidden_remainder_x
      - .offset:         108
        .size:           2
        .value_kind:     hidden_remainder_y
      - .offset:         110
        .size:           2
        .value_kind:     hidden_remainder_z
      - .offset:         128
        .size:           8
        .value_kind:     hidden_global_offset_x
      - .offset:         136
        .size:           8
        .value_kind:     hidden_global_offset_y
      - .offset:         144
        .size:           8
        .value_kind:     hidden_global_offset_z
      - .offset:         152
        .size:           2
        .value_kind:     hidden_grid_dims
    .group_segment_fixed_size: 61528
    .kernarg_segment_align: 8
    .kernarg_segment_size: 344
    .language:       OpenCL C
    .language_version:
      - 2
      - 0
    .max_flat_workgroup_size: 640
    .name:           _Z11p_gemm_mfmaPKfPKDv8_DF16_S0_S0_PDF16_PKiS6_PiS7_S7_S7_
    .private_segment_fixed_size: 0
    .sgpr_count:     36
    .sgpr_spill_count: 0
    .symbol:         _Z11p_gemm_mfmaPKfPKDv8_DF16_S0_S0_PDF16_PKiS6_PiS7_S7_S7_.kd
    .uniform_work_group_size: 1
    .uses_dynamic_stack: false
    .vgpr_count:     156
    .vgpr_spill_count: 0
    .wavefront_size: 64
  - .agpr_count:     0
    .args:
      - .actual_access:  read_only
        .address_space:  global
        .offset:         0
        .size:           8
        .value_kind:     global_buffer
      - .actual_access:  read_only
        .address_space:  global
        .offset:         8
        .size:           8
        .value_kind:     global_buffer
      - .actual_access:  read_only
        .address_space:  global
        .offset:         16
        .size:           8
        .value_kind:     global_buffer
      - .actual_access:  read_only
        .address_space:  global
        .offset:         24
        .size:           8
        .value_kind:     global_buffer
      - .actual_access:  read_only
        .address_space:  global
        .offset:         32
        .size:           8
        .value_kind:     global_buffer
      - .actual_access:  read_only
        .address_space:  global
        .offset:         40
        .size:           8
        .value_kind:     global_buffer
      - .actual_access:  read_only
        .address_space:  global
        .offset:         48
        .size:           8
        .value_kind:     global_buffer
      - .actual_access:  write_only
        .address_space:  global
        .offset:         56
        .size:           8
        .value_kind:     global_buffer
      - .actual_access:  write_only
        .address_space:  global
        .offset:         64
        .size:           8
        .value_kind:     global_buffer
      - .actual_access:  write_only
        .address_space:  global
        .offset:         72
        .size:           8
        .value_kind:     global_buffer
      - .actual_access:  write_only
        .address_space:  global
        .offset:         80
        .size:           8
        .value_kind:     global_buffer
      - .actual_access:  read_only
        .address_space:  global
        .offset:         88
        .size:           8
        .value_kind:     global_buffer
      - .actual_access:  write_only
        .address_space:  global
        .offset:         96
        .size:           8
        .value_kind:     global_buffer
      - .actual_access:  read_only
        .address_space:  global
        .offset:         104
        .size:           8
        .value_kind:     global_buffer
      - .actual_access:  read_only
        .address_space:  global
        .offset:         112
        .size:           8
        .value_kind:     global_buffer
      - .actual_access:  write_only
        .address_space:  global
        .offset:         120
        .size:           8
        .value_kind:     global_buffer
      - .actual_access:  read_only
        .address_space:  global
        .offset:         128
        .size:           8
        .value_kind:     global_buffer
      - .address_space:  global
        .offset:         136
        .size:           8
        .value_kind:     global_buffer
      - .address_space:  global
        .offset:         144
        .size:           8
        .value_kind:     global_buffer
      - .address_space:  global
        .offset:         152
        .size:           8
        .value_kind:     global_buffer
      - .address_space:  global
        .offset:         160
        .size:           8
        .value_kind:     global_buffer
      - .address_space:  global
        .offset:         168
        .size:           8
        .value_kind:     global_buffer
      - .offset:         176
        .size:           4
        .value_kind:     hidden_block_count_x
      - .offset:         180
        .size:           4
        .value_kind:     hidden_block_count_y
      - .offset:         184
        .size:           4
        .value_kind:     hidden_block_count_z
      - .offset:         188
        .size:           2
        .value_kind:     hidden_group_size_x
      - .offset:         190
        .size:           2
        .value_kind:     hidden_group_size_y
      - .offset:         192
        .size:           2
        .value_kind:     hidden_group_size_z
      - .offset:         194
        .size:           2
        .value_kind:     hidden_remainder_x
      - .offset:         196
        .size:           2
        .value_kind:     hidden_remainder_y
      - .offset:         198
        .size:           2
        .value_kind:     hidden_remainder_z
      - .offset:         216
        .size:           8
        .value_kind:     hidden_global_offset_x
      - .offset:         224
        .size:           8
        .value_kind:     hidden_global_offset_y
      - .offset:         232
        .size:           8
        .value_kind:     hidden_global_offset_z
      - .offset:         240
        .size:           2
        .value_kind:     hidden_grid_dims
    .group_segment_fixed_size: 1024
    .kernarg_segment_align: 8
    .kernarg_segment_size: 432
    .language:       OpenCL C
    .language_version:
      - 2
      - 0
    .max_flat_workgroup_size: 1024
    .name:           _Z12prep_weightsPKfS0_S0_S0_S0_S0_S0_PDF16_S1_S1_S1_S0_S1_S0_S0_PfPKiPiS5_S5_S5_S5_
    .private_segment_fixed_size: 0
    .sgpr_count:     48
    .sgpr_spill_count: 0
    .symbol:         _Z12prep_weightsPKfS0_S0_S0_S0_S0_S0_PDF16_S1_S1_S1_S0_S1_S0_S0_PfPKiPiS5_S5_S5_S5_.kd
    .uniform_work_group_size: 1
    .uses_dynamic_stack: false
    .vgpr_count:     29
    .vgpr_spill_count: 0
    .wavefront_size: 64
  - .agpr_count:     0
    .args:
      - .actual_access:  read_only
        .address_space:  global
        .offset:         0
        .size:           8
        .value_kind:     global_buffer
      - .actual_access:  read_only
        .address_space:  global
        .offset:         8
        .size:           8
        .value_kind:     global_buffer
      - .actual_access:  read_only
        .address_space:  global
        .offset:         16
        .size:           8
        .value_kind:     global_buffer
      - .actual_access:  read_only
        .address_space:  global
        .offset:         24
        .size:           8
        .value_kind:     global_buffer
      - .actual_access:  read_only
        .address_space:  global
        .offset:         32
        .size:           8
        .value_kind:     global_buffer
      - .actual_access:  read_only
        .address_space:  global
        .offset:         40
        .size:           8
        .value_kind:     global_buffer
      - .actual_access:  read_only
        .address_space:  global
        .offset:         48
        .size:           8
        .value_kind:     global_buffer
      - .actual_access:  read_only
        .address_space:  global
        .offset:         56
        .size:           8
        .value_kind:     global_buffer
      - .actual_access:  write_only
        .address_space:  global
        .offset:         64
        .size:           8
        .value_kind:     global_buffer
      - .actual_access:  read_only
        .address_space:  global
        .offset:         72
        .size:           8
        .value_kind:     global_buffer
      - .actual_access:  read_only
        .address_space:  global
        .offset:         80
        .size:           8
        .value_kind:     global_buffer
      - .actual_access:  read_only
        .address_space:  global
        .offset:         88
        .size:           8
        .value_kind:     global_buffer
      - .actual_access:  read_only
        .address_space:  global
        .offset:         96
        .size:           8
        .value_kind:     global_buffer
      - .actual_access:  read_only
        .address_space:  global
        .offset:         104
        .size:           8
        .value_kind:     global_buffer
    .group_segment_fixed_size: 160832
    .kernarg_segment_align: 8
    .kernarg_segment_size: 112
    .language:       OpenCL C
    .language_version:
      - 2
      - 0
    .max_flat_workgroup_size: 512
    .name:           _Z8gru_mfmaPKiPKDF16_PKDv8_DF16_S5_S5_S5_S0_S0_PfPKfS8_S8_S8_S0_
    .private_segment_fixed_size: 0
    .sgpr_count:     27
    .sgpr_spill_count: 0
    .symbol:         _Z8gru_mfmaPKiPKDF16_PKDv8_DF16_S5_S5_S5_S0_S0_PfPKfS8_S8_S8_S0_.kd
    .uniform_work_group_size: 1
    .uses_dynamic_stack: false
    .vgpr_count:     256
    .vgpr_spill_count: 0
    .wavefront_size: 64
  - .agpr_count:     0
    .args:
      - .actual_access:  read_only
        .address_space:  global
        .offset:         0
        .size:           8
        .value_kind:     global_buffer
      - .actual_access:  read_only
        .address_space:  global
        .offset:         8
        .size:           8
        .value_kind:     global_buffer
      - .actual_access:  read_only
        .address_space:  global
        .offset:         16
        .size:           8
        .value_kind:     global_buffer
      - .actual_access:  read_only
        .address_space:  global
        .offset:         24
        .size:           8
        .value_kind:     global_buffer
      - .actual_access:  read_only
        .address_space:  global
        .offset:         32
        .size:           8
        .value_kind:     global_buffer
      - .actual_access:  read_only
        .address_space:  global
        .offset:         40
        .size:           8
        .value_kind:     global_buffer
      - .actual_access:  read_only
        .address_space:  global
        .offset:         48
        .size:           8
        .value_kind:     global_buffer
      - .actual_access:  read_only
        .address_space:  global
        .offset:         56
        .size:           8
        .value_kind:     global_buffer
      - .actual_access:  write_only
        .address_space:  global
        .offset:         64
        .size:           8
        .value_kind:     global_buffer
    .group_segment_fixed_size: 26624
    .kernarg_segment_align: 8
    .kernarg_segment_size: 72
    .language:       OpenCL C
    .language_version:
      - 2
      - 0
    .max_flat_workgroup_size: 256
    .name:           _Z10gcn_kernelPKiS0_S0_S0_PKfS2_S2_S2_Pf
    .private_segment_fixed_size: 0
    .sgpr_count:     42
    .sgpr_spill_count: 0
    .symbol:         _Z10gcn_kernelPKiS0_S0_S0_PKfS2_S2_S2_Pf.kd
    .uniform_work_group_size: 1
    .uses_dynamic_stack: false
    .vgpr_count:     120
    .vgpr_spill_count: 0
    .wavefront_size: 64
